# baseline (speedup 1.0000x reference)
.Lk1_nowarm0:
	s_waitcnt lgkmcnt(0)
	s_add_u32 s8, s4, s17
	s_addc_u32 s9, s5, s20
	s_and_b32 s9, s9, 0xffff
	s_cmp_lg_u32 s21, 0
	s_cbranch_scc1 .Lk1_nokc
	s_mul_i32 s22, s15, 0x9c40
	s_mul_i32 s23, s16, 0x1388
	s_add_u32 s22, s22, s23
	v_mov_b32_e32 v3, s22
	v_lshl_add_u32 v3, v0, 6, v3
	global_load_dword v96, v3, s[6:7]
.Lk1_nokc:
	s_cmp_eq_u32 s21, 9
	s_cselect_b32 s17, 1, 0
	s_cmp_eq_u32 s16, 0
	s_cselect_b32 s17, s17, 0
	s_cmp_lg_u32 s17, 0
	s_cbranch_scc0 .Lk1_nowarm9
	s_mul_i32 s22, s15, 0x3a9800
	v_writelane_b32 v3, s22, 0
	s_add_u32 s23, s22, 0x10000
	v_writelane_b32 v3, s23, 1
	s_add_u32 s22, s22, 0x138800
	v_writelane_b32 v3, s22, 2
	s_add_u32 s23, s22, 0x10000
	v_writelane_b32 v3, s23, 3
	s_add_u32 s22, s22, 0x138800
	v_writelane_b32 v3, s22, 4
	s_add_u32 s23, s22, 0x10000
	v_writelane_b32 v3, s23, 5
	s_mov_b64 exec, 63
	global_load_dword v92, v3, s[32:33]
	s_mul_i32 s22, s15, 0x12c00
	s_add_u32 s22, s22, 0x1c200
	v_writelane_b32 v3, s22, 0
	s_add_u32 s22, s22, 0x10000
	v_writelane_b32 v3, s22, 1
	s_mul_i32 s22, s15, 0xe10
	v_writelane_b32 v3, s22, 2
	s_mul_i32 s22, s15, 0x4b0
	s_add_u32 s22, s22, 0x274200
	v_writelane_b32 v3, s22, 3
	s_mov_b64 exec, 15
	global_load_dword v93, v3, s[34:35]
	s_mov_b64 exec, s[18:19]
